# N2 router-weight staging to LDS: 16 serial load/wait/ds_write iterations replaced by 16 loads issued up front
# speedup vs baseline: 1.0123x; 1.0004x over previous
; #define LAS __attribute__((address_space(3)))
; __device__ __forceinline__ void n2_phase(const Args& a, int layer, const int wv, const bool dry = false) {
;     ...
;     __syncthreads();
;     for (int i4 = F.tid; i4 < DM * NEXP / 4; i4 += 512) *(LAS f32x4*)(rwl + 4 * i4) = *(const f32x4*)(rw + 4 * i4);
;     __syncthreads();
.LBB0_870:
	s_cmp_gt_i32 s28, 9
	s_cselect_b64 s[2:3], -1, 0
	s_cmp_lt_i32 s29, 10
	s_cselect_b64 s[4:5], -1, 0
	s_or_b64 s[2:3], s[2:3], s[4:5]
	s_and_b64 vcc, exec, s[2:3]
	s_cbranch_vccnz .LBB0_1208
	s_mov_b64 s[2:3], s[0:1]
	s_waitcnt vmcnt(0)
	v_mbcnt_lo_u32_b32 v0, -1, 0
	v_mbcnt_hi_u32_b32 v0, -1, v0
	s_mov_b32 s44, s18
	v_or_b32_e32 v0, s19, v0
	s_load_dword s4, s[30:31], 0x10
	s_waitcnt lgkmcnt(0)
	s_load_dword s6, s[30:31], 0x0
	v_readfirstlane_b32 s36, v0
	v_lshlrev_b32_e32 v40, 2, v0
	s_lshr_b32 s4, s4, 16
	s_cmp_lg_u32 s4, 0
	s_cselect_b64 s[4:5], -1, 0
	s_cmp_lg_u64 s[4:5], 0
	s_waitcnt lgkmcnt(0)
	s_addc_u32 s33, s6, 0
	s_mov_b32 s45, s33
	s_load_dwordx2 s[14:15], s[2:3], 0xf8
	s_waitcnt lgkmcnt(0)
	s_load_dwordx4 s[4:7], s[2:3], 0xc0
	s_load_dwordx2 s[16:17], s[2:3], 0x30
	s_movk_i32 s2, 0x2000
	v_cmp_gt_i32_e32 vcc, s2, v0
	s_waitcnt lgkmcnt(0)
	s_barrier
	s_and_saveexec_b64 s[2:3], vcc
	s_cbranch_execz .LBB0_874
	v_add_u32_e32 v1, 0xfffffe00, v0
	v_lshl_add_u32 v4, v0, 4, 0
	v_lshlrev_b32_e32 v2, 2, v0
	s_mov_b64 s[8:9], 0
	s_movk_i32 s10, 0x1dff
	v_lshlrev_b32_e32 v5, 4, v0
	global_load_dwordx4 v[44:47], v5, s[4:5]
	v_add_u32_e32 v5, 0x2000, v5
	global_load_dwordx4 v[48:51], v5, s[4:5]
	v_add_u32_e32 v5, 0x2000, v5
	global_load_dwordx4 v[52:55], v5, s[4:5]
	v_add_u32_e32 v5, 0x2000, v5
	global_load_dwordx4 v[56:59], v5, s[4:5]
	v_add_u32_e32 v5, 0x2000, v5
	global_load_dwordx4 v[60:63], v5, s[4:5]
	v_add_u32_e32 v5, 0x2000, v5
	global_load_dwordx4 v[64:67], v5, s[4:5]
	v_add_u32_e32 v5, 0x2000, v5
	global_load_dwordx4 v[68:71], v5, s[4:5]
	v_add_u32_e32 v5, 0x2000, v5
	global_load_dwordx4 v[72:75], v5, s[4:5]
	v_add_u32_e32 v5, 0x2000, v5
	global_load_dwordx4 v[76:79], v5, s[4:5]
	v_add_u32_e32 v5, 0x2000, v5
	global_load_dwordx4 v[80:83], v5, s[4:5]
	v_add_u32_e32 v5, 0x2000, v5
	global_load_dwordx4 v[84:87], v5, s[4:5]
	v_add_u32_e32 v5, 0x2000, v5
	global_load_dwordx4 v[88:91], v5, s[4:5]
	v_add_u32_e32 v5, 0x2000, v5
	global_load_dwordx4 v[92:95], v5, s[4:5]
	v_add_u32_e32 v5, 0x2000, v5
	global_load_dwordx4 v[96:99], v5, s[4:5]
	v_add_u32_e32 v5, 0x2000, v5
	global_load_dwordx4 v[100:103], v5, s[4:5]
	v_add_u32_e32 v5, 0x2000, v5
	global_load_dwordx4 v[104:107], v5, s[4:5]
	v_add_u32_e32 v9, 0x10000, v4
	s_waitcnt vmcnt(15)
	ds_write_b128 v4, v[44:47]
	s_waitcnt vmcnt(14)
	ds_write_b128 v4, v[48:51] offset:8192
	s_waitcnt vmcnt(13)
	ds_write_b128 v4, v[52:55] offset:16384
	s_waitcnt vmcnt(12)
	ds_write_b128 v4, v[56:59] offset:24576
	s_waitcnt vmcnt(11)
	ds_write_b128 v4, v[60:63] offset:32768
	s_waitcnt vmcnt(10)
	ds_write_b128 v4, v[64:67] offset:40960
	s_waitcnt vmcnt(9)
	ds_write_b128 v4, v[68:71] offset:49152
	s_waitcnt vmcnt(8)
	ds_write_b128 v4, v[72:75] offset:57344
	s_waitcnt vmcnt(7)
	ds_write_b128 v9, v[76:79]
	s_waitcnt vmcnt(6)
	ds_write_b128 v9, v[80:83] offset:8192
	s_waitcnt vmcnt(5)
	ds_write_b128 v9, v[84:87] offset:16384
	s_waitcnt vmcnt(4)
	ds_write_b128 v9, v[88:91] offset:24576
	s_waitcnt vmcnt(3)
	ds_write_b128 v9, v[92:95] offset:32768
	s_waitcnt vmcnt(2)
	ds_write_b128 v9, v[96:99] offset:40960
	s_waitcnt vmcnt(1)
	ds_write_b128 v9, v[100:103] offset:49152
	s_waitcnt vmcnt(0)
	ds_write_b128 v9, v[104:107] offset:57344

; #define LAS __attribute__((address_space(3)))
; __device__ __forceinline__ void n2_phase(const Args& a, int layer, const int wv, const bool dry = false) {
;     ...
;     __syncthreads();
;     for (int i4 = F.tid; i4 < DM * NEXP / 4; i4 += 512) *(LAS f32x4*)(rwl + 4 * i4) = *(const f32x4*)(rw + 4 * i4);
;     __syncthreads();
.LBB0_1974:
	s_cmp_gt_i32 s28, 21
	s_cselect_b64 s[2:3], -1, 0
	s_cmp_lt_i32 s29, 22
	s_cselect_b64 s[4:5], -1, 0
	s_or_b64 s[2:3], s[2:3], s[4:5]
	s_and_b64 vcc, exec, s[2:3]
	s_cbranch_vccnz .LBB0_2312
	s_mov_b64 s[8:9], s[0:1]
	s_waitcnt vmcnt(0)
	v_mbcnt_lo_u32_b32 v0, -1, 0
	v_mbcnt_hi_u32_b32 v0, -1, v0
	s_mov_b32 s44, s18
	v_or_b32_e32 v0, s19, v0
	s_load_dword s2, s[30:31], 0x10
	s_load_dword s4, s[30:31], 0x0
	v_readfirstlane_b32 s36, v0
	v_lshlrev_b32_e32 v40, 2, v0
	s_waitcnt lgkmcnt(0)
	s_lshr_b32 s2, s2, 16
	s_cmp_lg_u32 s2, 0
	s_cselect_b64 s[2:3], -1, 0
	s_cmp_lg_u64 s[2:3], 0
	s_addc_u32 s33, s4, 0
	s_mov_b32 s45, s33
	s_load_dwordx2 s[14:15], s[8:9], 0xf8
	s_waitcnt lgkmcnt(0)
	s_load_dwordx4 s[4:7], s[8:9], 0xc0
	s_load_dwordx2 s[2:3], s[8:9], 0x30
	s_movk_i32 s8, 0x2000
	v_cmp_gt_i32_e32 vcc, s8, v0
	s_waitcnt lgkmcnt(0)
	s_barrier
	s_and_saveexec_b64 s[8:9], vcc
	s_cbranch_execz .LBB0_1978
	s_add_u32 s4, s4, 0x20000
	s_addc_u32 s5, s5, 0
	v_add_u32_e32 v1, 0xfffffe00, v0
	v_lshl_add_u32 v4, v0, 4, 0
	v_lshlrev_b32_e32 v2, 2, v0
	s_mov_b64 s[10:11], 0
	s_movk_i32 s12, 0x1dff
	v_lshlrev_b32_e32 v5, 4, v0
	global_load_dwordx4 v[44:47], v5, s[4:5]
	v_add_u32_e32 v5, 0x2000, v5
	global_load_dwordx4 v[48:51], v5, s[4:5]
	v_add_u32_e32 v5, 0x2000, v5
	global_load_dwordx4 v[52:55], v5, s[4:5]
	v_add_u32_e32 v5, 0x2000, v5
	global_load_dwordx4 v[56:59], v5, s[4:5]
	v_add_u32_e32 v5, 0x2000, v5
	global_load_dwordx4 v[60:63], v5, s[4:5]
	v_add_u32_e32 v5, 0x2000, v5
	global_load_dwordx4 v[64:67], v5, s[4:5]
	v_add_u32_e32 v5, 0x2000, v5
	global_load_dwordx4 v[68:71], v5, s[4:5]
	v_add_u32_e32 v5, 0x2000, v5
	global_load_dwordx4 v[72:75], v5, s[4:5]
	v_add_u32_e32 v5, 0x2000, v5
	global_load_dwordx4 v[76:79], v5, s[4:5]
	v_add_u32_e32 v5, 0x2000, v5
	global_load_dwordx4 v[80:83], v5, s[4:5]
	v_add_u32_e32 v5, 0x2000, v5
	global_load_dwordx4 v[84:87], v5, s[4:5]
	v_add_u32_e32 v5, 0x2000, v5
	global_load_dwordx4 v[88:91], v5, s[4:5]
	v_add_u32_e32 v5, 0x2000, v5
	global_load_dwordx4 v[92:95], v5, s[4:5]
	v_add_u32_e32 v5, 0x2000, v5
	global_load_dwordx4 v[96:99], v5, s[4:5]
	v_add_u32_e32 v5, 0x2000, v5
	global_load_dwordx4 v[100:103], v5, s[4:5]
	v_add_u32_e32 v5, 0x2000, v5
	global_load_dwordx4 v[104:107], v5, s[4:5]
	v_add_u32_e32 v9, 0x10000, v4
	s_waitcnt vmcnt(15)
	ds_write_b128 v4, v[44:47]
	s_waitcnt vmcnt(14)
	ds_write_b128 v4, v[48:51] offset:8192
	s_waitcnt vmcnt(13)
	ds_write_b128 v4, v[52:55] offset:16384
	s_waitcnt vmcnt(12)
	ds_write_b128 v4, v[56:59] offset:24576
	s_waitcnt vmcnt(11)
	ds_write_b128 v4, v[60:63] offset:32768
	s_waitcnt vmcnt(10)
	ds_write_b128 v4, v[64:67] offset:40960
	s_waitcnt vmcnt(9)
	ds_write_b128 v4, v[68:71] offset:49152
	s_waitcnt vmcnt(8)
	ds_write_b128 v4, v[72:75] offset:57344
	s_waitcnt vmcnt(7)
	ds_write_b128 v9, v[76:79]
	s_waitcnt vmcnt(6)
	ds_write_b128 v9, v[80:83] offset:8192
	s_waitcnt vmcnt(5)
	ds_write_b128 v9, v[84:87] offset:16384
	s_waitcnt vmcnt(4)
	ds_write_b128 v9, v[88:91] offset:24576
	s_waitcnt vmcnt(3)
	ds_write_b128 v9, v[92:95] offset:32768
	s_waitcnt vmcnt(2)
	ds_write_b128 v9, v[96:99] offset:40960
	s_waitcnt vmcnt(1)
	ds_write_b128 v9, v[100:103] offset:49152
	s_waitcnt vmcnt(0)
	ds_write_b128 v9, v[104:107] offset:57344

; #define LAS __attribute__((address_space(3)))
; __device__ __forceinline__ void n2_phase(const Args& a, int layer, const int wv, const bool dry = false) {
;     ...
;     __syncthreads();
;     for (int i4 = F.tid; i4 < DM * NEXP / 4; i4 += 512) *(LAS f32x4*)(rwl + 4 * i4) = *(const f32x4*)(rw + 4 * i4);
;     __syncthreads();
.LBB0_3345:
	s_cmp_gt_i32 s28, 33
	s_cselect_b64 s[2:3], -1, 0
	s_cmp_lt_i32 s29, 34
	s_cselect_b64 s[4:5], -1, 0
	s_or_b64 s[2:3], s[2:3], s[4:5]
	s_and_b64 vcc, exec, s[2:3]
	s_cbranch_vccnz .LBB0_3683
	s_mov_b64 s[8:9], s[0:1]
	s_waitcnt vmcnt(0)
	v_mbcnt_lo_u32_b32 v0, -1, 0
	v_mbcnt_hi_u32_b32 v0, -1, v0
	s_mov_b32 s44, s18
	v_or_b32_e32 v0, s19, v0
	s_load_dword s2, s[30:31], 0x10
	s_load_dword s4, s[30:31], 0x0
	v_readfirstlane_b32 s36, v0
	v_lshlrev_b32_e32 v40, 2, v0
	s_waitcnt lgkmcnt(0)
	s_lshr_b32 s2, s2, 16
	s_cmp_lg_u32 s2, 0
	s_cselect_b64 s[2:3], -1, 0
	s_cmp_lg_u64 s[2:3], 0
	s_addc_u32 s33, s4, 0
	s_mov_b32 s45, s33
	s_load_dwordx2 s[14:15], s[8:9], 0xf8
	s_waitcnt lgkmcnt(0)
	s_load_dwordx4 s[4:7], s[8:9], 0xc0
	s_load_dwordx2 s[2:3], s[8:9], 0x30
	s_movk_i32 s8, 0x2000
	v_cmp_gt_i32_e32 vcc, s8, v0
	s_waitcnt lgkmcnt(0)
	s_barrier
	s_and_saveexec_b64 s[8:9], vcc
	s_cbranch_execz .LBB0_3349
	s_add_u32 s4, s4, 0x40000
	s_addc_u32 s5, s5, 0
	v_add_u32_e32 v1, 0xfffffe00, v0
	v_lshl_add_u32 v4, v0, 4, 0
	v_lshlrev_b32_e32 v2, 2, v0
	s_mov_b64 s[10:11], 0
	s_movk_i32 s12, 0x1dff
	v_lshlrev_b32_e32 v5, 4, v0
	global_load_dwordx4 v[44:47], v5, s[4:5]
	v_add_u32_e32 v5, 0x2000, v5
	global_load_dwordx4 v[48:51], v5, s[4:5]
	v_add_u32_e32 v5, 0x2000, v5
	global_load_dwordx4 v[52:55], v5, s[4:5]
	v_add_u32_e32 v5, 0x2000, v5
	global_load_dwordx4 v[56:59], v5, s[4:5]
	v_add_u32_e32 v5, 0x2000, v5
	global_load_dwordx4 v[60:63], v5, s[4:5]
	v_add_u32_e32 v5, 0x2000, v5
	global_load_dwordx4 v[64:67], v5, s[4:5]
	v_add_u32_e32 v5, 0x2000, v5
	global_load_dwordx4 v[68:71], v5, s[4:5]
	v_add_u32_e32 v5, 0x2000, v5
	global_load_dwordx4 v[72:75], v5, s[4:5]
	v_add_u32_e32 v5, 0x2000, v5
	global_load_dwordx4 v[76:79], v5, s[4:5]
	v_add_u32_e32 v5, 0x2000, v5
	global_load_dwordx4 v[80:83], v5, s[4:5]
	v_add_u32_e32 v5, 0x2000, v5
	global_load_dwordx4 v[84:87], v5, s[4:5]
	v_add_u32_e32 v5, 0x2000, v5
	global_load_dwordx4 v[88:91], v5, s[4:5]
	v_add_u32_e32 v5, 0x2000, v5
	global_load_dwordx4 v[92:95], v5, s[4:5]
	v_add_u32_e32 v5, 0x2000, v5
	global_load_dwordx4 v[96:99], v5, s[4:5]
	v_add_u32_e32 v5, 0x2000, v5
	global_load_dwordx4 v[100:103], v5, s[4:5]
	v_add_u32_e32 v5, 0x2000, v5
	global_load_dwordx4 v[104:107], v5, s[4:5]
	v_add_u32_e32 v9, 0x10000, v4
	s_waitcnt vmcnt(15)
	ds_write_b128 v4, v[44:47]
	s_waitcnt vmcnt(14)
	ds_write_b128 v4, v[48:51] offset:8192
	s_waitcnt vmcnt(13)
	ds_write_b128 v4, v[52:55] offset:16384
	s_waitcnt vmcnt(12)
	ds_write_b128 v4, v[56:59] offset:24576
	s_waitcnt vmcnt(11)
	ds_write_b128 v4, v[60:63] offset:32768
	s_waitcnt vmcnt(10)
	ds_write_b128 v4, v[64:67] offset:40960
	s_waitcnt vmcnt(9)
	ds_write_b128 v4, v[68:71] offset:49152
	s_waitcnt vmcnt(8)
	ds_write_b128 v4, v[72:75] offset:57344
	s_waitcnt vmcnt(7)
	ds_write_b128 v9, v[76:79]
	s_waitcnt vmcnt(6)
	ds_write_b128 v9, v[80:83] offset:8192
	s_waitcnt vmcnt(5)
	ds_write_b128 v9, v[84:87] offset:16384
	s_waitcnt vmcnt(4)
	ds_write_b128 v9, v[88:91] offset:24576
	s_waitcnt vmcnt(3)
	ds_write_b128 v9, v[92:95] offset:32768
	s_waitcnt vmcnt(2)
	ds_write_b128 v9, v[96:99] offset:40960
	s_waitcnt vmcnt(1)
	ds_write_b128 v9, v[100:103] offset:49152
	s_waitcnt vmcnt(0)
	ds_write_b128 v9, v[104:107] offset:57344

; #define LAS __attribute__((address_space(3)))
; __device__ __forceinline__ void n2_phase(const Args& a, int layer, const int wv, const bool dry = false) {
;     ...
;     __syncthreads();
;     for (int i4 = F.tid; i4 < DM * NEXP / 4; i4 += 512) *(LAS f32x4*)(rwl + 4 * i4) = *(const f32x4*)(rw + 4 * i4);
;     __syncthreads();
.LBB0_4449:
	s_cmp_gt_i32 s28, 45
	s_cselect_b64 s[2:3], -1, 0
	s_cmp_lt_i32 s29, 46
	s_cselect_b64 s[4:5], -1, 0
	s_or_b64 s[2:3], s[2:3], s[4:5]
	s_and_b64 vcc, exec, s[2:3]
	s_cbranch_vccnz .LBB0_4787
	s_mov_b64 s[8:9], s[0:1]
	s_waitcnt vmcnt(0)
	v_mbcnt_lo_u32_b32 v0, -1, 0
	v_mbcnt_hi_u32_b32 v0, -1, v0
	s_mov_b32 s44, s18
	v_or_b32_e32 v0, s19, v0
	s_load_dword s2, s[30:31], 0x10
	s_load_dword s4, s[30:31], 0x0
	v_readfirstlane_b32 s36, v0
	v_lshlrev_b32_e32 v40, 2, v0
	s_waitcnt lgkmcnt(0)
	s_lshr_b32 s2, s2, 16
	s_cmp_lg_u32 s2, 0
	s_cselect_b64 s[2:3], -1, 0
	s_cmp_lg_u64 s[2:3], 0
	s_addc_u32 s33, s4, 0
	s_mov_b32 s45, s33
	s_load_dwordx2 s[14:15], s[8:9], 0xf8
	s_waitcnt lgkmcnt(0)
	s_load_dwordx4 s[4:7], s[8:9], 0xc0
	s_load_dwordx2 s[2:3], s[8:9], 0x30
	s_movk_i32 s8, 0x2000
	v_cmp_gt_i32_e32 vcc, s8, v0
	s_waitcnt lgkmcnt(0)
	s_barrier
	s_and_saveexec_b64 s[8:9], vcc
	s_cbranch_execz .LBB0_4453
	s_add_u32 s4, s4, 0x60000
	s_addc_u32 s5, s5, 0
	v_add_u32_e32 v1, 0xfffffe00, v0
	v_lshl_add_u32 v4, v0, 4, 0
	v_lshlrev_b32_e32 v2, 2, v0
	s_mov_b64 s[10:11], 0
	s_movk_i32 s12, 0x1dff
	v_lshlrev_b32_e32 v5, 4, v0
	global_load_dwordx4 v[44:47], v5, s[4:5]
	v_add_u32_e32 v5, 0x2000, v5
	global_load_dwordx4 v[48:51], v5, s[4:5]
	v_add_u32_e32 v5, 0x2000, v5
	global_load_dwordx4 v[52:55], v5, s[4:5]
	v_add_u32_e32 v5, 0x2000, v5
	global_load_dwordx4 v[56:59], v5, s[4:5]
	v_add_u32_e32 v5, 0x2000, v5
	global_load_dwordx4 v[60:63], v5, s[4:5]
	v_add_u32_e32 v5, 0x2000, v5
	global_load_dwordx4 v[64:67], v5, s[4:5]
	v_add_u32_e32 v5, 0x2000, v5
	global_load_dwordx4 v[68:71], v5, s[4:5]
	v_add_u32_e32 v5, 0x2000, v5
	global_load_dwordx4 v[72:75], v5, s[4:5]
	v_add_u32_e32 v5, 0x2000, v5
	global_load_dwordx4 v[76:79], v5, s[4:5]
	v_add_u32_e32 v5, 0x2000, v5
	global_load_dwordx4 v[80:83], v5, s[4:5]
	v_add_u32_e32 v5, 0x2000, v5
	global_load_dwordx4 v[84:87], v5, s[4:5]
	v_add_u32_e32 v5, 0x2000, v5
	global_load_dwordx4 v[88:91], v5, s[4:5]
	v_add_u32_e32 v5, 0x2000, v5
	global_load_dwordx4 v[92:95], v5, s[4:5]
	v_add_u32_e32 v5, 0x2000, v5
	global_load_dwordx4 v[96:99], v5, s[4:5]
	v_add_u32_e32 v5, 0x2000, v5
	global_load_dwordx4 v[100:103], v5, s[4:5]
	v_add_u32_e32 v5, 0x2000, v5
	global_load_dwordx4 v[104:107], v5, s[4:5]
	v_add_u32_e32 v9, 0x10000, v4
	s_waitcnt vmcnt(15)
	ds_write_b128 v4, v[44:47]
	s_waitcnt vmcnt(14)
	ds_write_b128 v4, v[48:51] offset:8192
	s_waitcnt vmcnt(13)
	ds_write_b128 v4, v[52:55] offset:16384
	s_waitcnt vmcnt(12)
	ds_write_b128 v4, v[56:59] offset:24576
	s_waitcnt vmcnt(11)
	ds_write_b128 v4, v[60:63] offset:32768
	s_waitcnt vmcnt(10)
	ds_write_b128 v4, v[64:67] offset:40960
	s_waitcnt vmcnt(9)
	ds_write_b128 v4, v[68:71] offset:49152
	s_waitcnt vmcnt(8)
	ds_write_b128 v4, v[72:75] offset:57344
	s_waitcnt vmcnt(7)
	ds_write_b128 v9, v[76:79]
	s_waitcnt vmcnt(6)
	ds_write_b128 v9, v[80:83] offset:8192
	s_waitcnt vmcnt(5)
	ds_write_b128 v9, v[84:87] offset:16384
	s_waitcnt vmcnt(4)
	ds_write_b128 v9, v[88:91] offset:24576
	s_waitcnt vmcnt(3)
	ds_write_b128 v9, v[92:95] offset:32768
	s_waitcnt vmcnt(2)
	ds_write_b128 v9, v[96:99] offset:40960
	s_waitcnt vmcnt(1)
	ds_write_b128 v9, v[100:103] offset:49152
	s_waitcnt vmcnt(0)
	ds_write_b128 v9, v[104:107] offset:57344
